# fp8 expert GEMM epilogues: output scales folded into the MFMA block-scale exponent (exact powers of two), dead zero-inits removed, SwiGLU epilogue rewritten 8 values side by side
# speedup vs baseline: 1.0083x; 1.0083x over previous
; #define LAS __attribute__((address_space(3)))
; __device__ __forceinline__ int lane_id() { unsigned z = 0u; asm volatile("" : "+v"(z)); return (int)__builtin_amdgcn_mbcnt_hi(~0u, __builtin_amdgcn_mbcnt_lo(~0u, z)); }
; #define REP(j) for (int rep_ = 0; rep_ < 1 + (((REPMASK) >> (j)) & 1); ++rep_)
; __global__ void __launch_bounds__(NTHR, 2) fwd(Args args) {
;     ...
;         if (EN(7) && IN(pb + 7)) {
;             PHASE_ENV();
;             LAS int* tp = (LAS int*)(Fp.lds + LDS_MISC - 512);
;             { int t_ = Fp.wave * 64 + lane_id(); asm volatile("" : "+v"(t_)); if (t_ < 66) tp[t_] = ETAB_[t_]; }
;             __syncthreads();
;             if (l >= FP8_FIRST) {
;                 gm::Gemm g{X1Q_, ws + WS_WGU + (size_t)l * NE1 * 1024 * D * 2, D, ROWTOK_, (size_t)1024 * D};
;                 gm::GroupOrder S{tp, 4, Fp.G, Fp.vcu, 0};
;                 gm::EpiSwiGlu<(DOWN_FP8 != 0)> E{HB_, 1.0f / W8SCALE};
;                 REP(7) { S.ecur = 0; gm::gemm_phase<gm::EpiSwiGlu<(DOWN_FP8 != 0)>, gm::GroupOrder, true, true>(Fp.lds, Fp.wave, g, S, E); }
.LBB0_1063:
	s_andn2_b64 vcc, exec, s[4:5]
	s_cbranch_vccnz .LBB0_1137
	v_mov_b32_e32 v251, 0x7a7a7a7a
	v_readlane_b32 s4, v255, 8
	v_readlane_b32 s5, v255, 9
	v_readlane_b32 s12, v255, 7
	v_readlane_b32 s2, v255, 2
	v_readlane_b32 s22, v255, 4
	s_waitcnt vmcnt(0)
	v_mov_b32_e32 v0, v193
	s_load_dwordx2 s[44:45], s[4:5], 0x118
	s_movk_i32 s4, 0x42
	v_mbcnt_lo_u32_b32 v0, -1, v0
	v_mbcnt_hi_u32_b32 v0, -1, v0
	v_lshl_add_u32 v0, s12, 6, v0
	s_nop 0
	v_cmp_gt_i32_e32 vcc, s4, v0
	s_and_saveexec_b64 s[4:5], vcc
	s_cbranch_execz .LBB0_1066
	v_lshl_add_u32 v1, v0, 2, 0
	v_add_u32_e32 v2, 0x23d00, v1
	v_ashrrev_i32_e32 v1, 31, v0
	s_waitcnt lgkmcnt(0)
	v_lshl_add_u64 v[0:1], v[0:1], 2, s[44:45]
	v_add_co_u32_e32 v0, vcc, 0x100000, v0
	s_nop 1
	v_addc_co_u32_e32 v1, vcc, 0, v1, vcc
	global_load_dword v0, v[0:1], off
	s_waitcnt vmcnt(0)
	ds_write_b32 v2, v0

; #define PG8_STAGE(bufoff, gbase, voff) do { _Pragma("unroll") for (int _i = 0; _i < 2; ++_i) \
;         __builtin_amdgcn_global_load_lds((const unsigned*)((const char*)(gbase) + (voff)[_i]), (LAS unsigned*)(lds + (bufoff) + ldsw + _i * 8192), 16, 0, 0); } while (0)
; #define PG8_LDA(dst, b, h) do { _Pragma("unroll") for (int m = 0; m < 4; ++m) _Pragma("unroll") for (int k = 0; k < 2; ++k) dst[m][k] = *(const LAS bf16x8*)(lds + PG8_SA(b, h) + aoff + m * 2048 + k * KOFF); } while (0)
; #define PG8_LDB(dst, b, h) do { _Pragma("unroll") for (int n = 0; n < 2; ++n) _Pragma("unroll") for (int k = 0; k < 2; ++k) dst[n][k] = *(const LAS bf16x8*)(lds + PG8_SB(b, h) + boff + n * 2048 + k * KOFF); } while (0)
; #define PG8_WAIT_V(n) asm volatile("s_waitcnt vmcnt(" #n ")" ::: "memory")
; #define PG8_WAIT_L(n) asm volatile("s_waitcnt lgkmcnt(" #n ")" ::: "memory")
; #define PG8_BAR __builtin_amdgcn_s_barrier()
; #define PG8_SCHED __builtin_amdgcn_sched_barrier(0)
; #define PG8_AOFF(u_, o0, o1) do { _Pragma("unroll") for (int _i = 0; _i < 2; ++_i) { const int r0 = (u_).pm * BM + Rr[_i], r1 = r0 + HALF; \
;         const int g0 = GATHER ? g.rowidx[r0] : r0, g1 = GATHER ? g.rowidx[r1] : r1; \
;         o0[_i] = (unsigned)g0 * (unsigned)K + (unsigned)Cc[_i]; o1[_i] = (unsigned)g1 * (unsigned)K + (unsigned)Cc[_i]; } } while (0)
; template <class Epi, class Sched, bool GATHER, bool FP8 = false, bool ALIGN = true>
; __device__ __forceinline__ void gemm_phase(LAS unsigned char* lds, int wave, const Gemm g, const Sched& S, const Epi& E) {
;     ...
;             PG8_LDB(B0, 0, 0); PG8_LDB(B1, 0, 1); PG8_SCHED; PG8_LDA(At, 0, 0); PG8_STAGE(PG8_SA(1, 1), a1, ca1);
;             if (last && has_next) PG8_AOFF(nxt, ca0, ca1);
;             PG8_WAIT_V(8); PG8_WAIT_L(0); PG8_BAR; PG8_MMA(0, 0, At, B0); PG8_MMA(0, 1, At, B1); PG8_BAR; PG8_SCHED;
;             PG8_LDA(At, 0, 1); PG8_STAGE(PG8_SB(0, 0), b2, voffB0); PG8_STAGE(PG8_SB(0, 1), b2, voffB1); PG8_STAGE(PG8_SA(0, 0), a2, ca0);
;             PG8_WAIT_V(8); PG8_WAIT_L(0); PG8_BAR; PG8_MMA(1, 0, At, B0); PG8_MMA(1, 1, At, B1); PG8_BAR; PG8_SCHED;
.LBB0_1080:
	s_waitcnt vmcnt(8)
	s_add_u32 s14, s10, 0x80
	s_waitcnt lgkmcnt(0)
	s_addc_u32 s15, s11, 0
	s_and_b64 s[12:13], s[12:13], exec
	v_mov_b32_e32 v217, v193
	s_cselect_b32 s13, s7, s15
	s_cselect_b32 s12, s6, s14
	s_cselect_b32 s15, s5, s82
	s_cselect_b32 s14, s9, s49
	s_barrier
	s_setprio 1
	s_waitcnt lgkmcnt(0)
	v_mfma_scale_f32_16x16x128_f8f6f4 v[188:191], v[16:23], v[56:63], v[188:191], v252, v251 op_sel_hi:[0,0,0]
	v_mfma_scale_f32_16x16x128_f8f6f4 v[180:183], v[24:31], v[56:63], v[180:183], v252, v251 op_sel_hi:[0,0,0]
	v_mfma_scale_f32_16x16x128_f8f6f4 v[172:175], v[16:23], v[48:55], v[172:175], v252, v251 op_sel_hi:[0,0,0]
	v_mfma_scale_f32_16x16x128_f8f6f4 v[164:167], v[24:31], v[48:55], v[164:167], v252, v251 op_sel_hi:[0,0,0]
	v_mfma_scale_f32_16x16x128_f8f6f4 v[156:159], v[16:23], v[40:47], v[156:159], v252, v251 op_sel_hi:[0,0,0]
	v_mfma_scale_f32_16x16x128_f8f6f4 v[148:151], v[24:31], v[40:47], v[148:151], v252, v251 op_sel_hi:[0,0,0]
	v_mfma_scale_f32_16x16x128_f8f6f4 v[140:143], v[16:23], v[32:39], v[140:143], v252, v251 op_sel_hi:[0,0,0]
	v_mfma_scale_f32_16x16x128_f8f6f4 v[132:135], v[24:31], v[32:39], v[132:135], v252, v251 op_sel_hi:[0,0,0]
	s_setprio 0
	s_setprio 1
	v_mfma_scale_f32_16x16x128_f8f6f4 v[184:187], v[0:7], v[56:63], v[184:187], v252, v251 op_sel_hi:[0,0,0]
	v_mfma_scale_f32_16x16x128_f8f6f4 v[176:179], v[8:15], v[56:63], v[176:179], v252, v251 op_sel_hi:[0,0,0]
	v_mfma_scale_f32_16x16x128_f8f6f4 v[168:171], v[0:7], v[48:55], v[168:171], v252, v251 op_sel_hi:[0,0,0]
	v_mfma_scale_f32_16x16x128_f8f6f4 v[160:163], v[8:15], v[48:55], v[160:163], v252, v251 op_sel_hi:[0,0,0]
	v_mfma_scale_f32_16x16x128_f8f6f4 v[152:155], v[0:7], v[40:47], v[152:155], v252, v251 op_sel_hi:[0,0,0]
	v_mfma_scale_f32_16x16x128_f8f6f4 v[144:147], v[8:15], v[40:47], v[144:147], v252, v251 op_sel_hi:[0,0,0]
	v_mfma_scale_f32_16x16x128_f8f6f4 v[136:139], v[0:7], v[32:39], v[136:139], v252, v251 op_sel_hi:[0,0,0]
	v_mfma_scale_f32_16x16x128_f8f6f4 v[128:131], v[8:15], v[32:39], v[128:131], v252, v251 op_sel_hi:[0,0,0]
	s_setprio 0
	s_barrier
	s_mov_b32 m0, s34
	v_lshl_add_u64 v[196:197], s[14:15], 0, v[204:205]
	ds_read_b128 v[32:35], v238 offset:16384
	ds_read_b128 v[36:39], v238 offset:17408
	ds_read_b128 v[40:43], v238 offset:18432
	ds_read_b128 v[44:47], v238 offset:19456
	ds_read_b128 v[48:51], v238 offset:20480
	ds_read_b128 v[52:55], v238 offset:21504
	ds_read_b128 v[56:59], v238 offset:22528
	ds_read_b128 v[60:63], v238 offset:23552
	global_load_lds_dwordx4 v[196:197], off
	v_lshl_add_u64 v[198:199], s[14:15], 0, v[208:209]
	s_mov_b32 m0, s35
	v_lshl_add_u64 v[200:201], s[14:15], 0, v[206:207]
	global_load_lds_dwordx4 v[198:199], off
	s_mov_b32 m0, s40
	v_lshl_add_u64 v[202:203], s[14:15], 0, v[210:211]
	global_load_lds_dwordx4 v[200:201], off
	s_mov_b32 m0, s41
	v_mov_b32_e32 v215, v193
	global_load_lds_dwordx4 v[202:203], off
	s_mov_b32 m0, s31
	v_lshl_add_u64 v[226:227], s[12:13], 0, v[192:193]
	global_load_lds_dwordx4 v192, s[12:13]
	s_mov_b32 m0, s53
	v_lshl_add_u64 v[228:229], s[12:13], 0, v[214:215]
	global_load_lds_dwordx4 v214, s[12:13]
	s_waitcnt vmcnt(8)
	s_waitcnt lgkmcnt(0)
	s_barrier
	s_setprio 1
	s_waitcnt lgkmcnt(0)
	v_mfma_scale_f32_16x16x128_f8f6f4 v[124:127], v[16:23], v[32:39], v[124:127], v252, v251 op_sel_hi:[0,0,0]
	v_mfma_scale_f32_16x16x128_f8f6f4 v[116:119], v[24:31], v[32:39], v[116:119], v252, v251 op_sel_hi:[0,0,0]
	v_mfma_scale_f32_16x16x128_f8f6f4 v[108:111], v[16:23], v[40:47], v[108:111], v252, v251 op_sel_hi:[0,0,0]
	v_mfma_scale_f32_16x16x128_f8f6f4 v[100:103], v[24:31], v[40:47], v[100:103], v252, v251 op_sel_hi:[0,0,0]
	v_mfma_scale_f32_16x16x128_f8f6f4 v[92:95], v[16:23], v[48:55], v[92:95], v252, v251 op_sel_hi:[0,0,0]
	v_mfma_scale_f32_16x16x128_f8f6f4 v[84:87], v[24:31], v[48:55], v[84:87], v252, v251 op_sel_hi:[0,0,0]
	v_mfma_scale_f32_16x16x128_f8f6f4 v[76:79], v[16:23], v[56:63], v[76:79], v252, v251 op_sel_hi:[0,0,0]
	v_mfma_scale_f32_16x16x128_f8f6f4 v[68:71], v[24:31], v[56:63], v[68:71], v252, v251 op_sel_hi:[0,0,0]
	s_setprio 0
	s_setprio 1
	v_mfma_scale_f32_16x16x128_f8f6f4 v[120:123], v[0:7], v[32:39], v[120:123], v252, v251 op_sel_hi:[0,0,0]
	v_mfma_scale_f32_16x16x128_f8f6f4 v[112:115], v[8:15], v[32:39], v[112:115], v252, v251 op_sel_hi:[0,0,0]
	v_mfma_scale_f32_16x16x128_f8f6f4 v[104:107], v[0:7], v[40:47], v[104:107], v252, v251 op_sel_hi:[0,0,0]
	v_mfma_scale_f32_16x16x128_f8f6f4 v[96:99], v[8:15], v[40:47], v[96:99], v252, v251 op_sel_hi:[0,0,0]
	v_mfma_scale_f32_16x16x128_f8f6f4 v[88:91], v[0:7], v[48:55], v[88:91], v252, v251 op_sel_hi:[0,0,0]
	v_mfma_scale_f32_16x16x128_f8f6f4 v[80:83], v[8:15], v[48:55], v[80:83], v252, v251 op_sel_hi:[0,0,0]
	v_mfma_scale_f32_16x16x128_f8f6f4 v[72:75], v[0:7], v[56:63], v[72:75], v252, v251 op_sel_hi:[0,0,0]
	v_mfma_scale_f32_16x16x128_f8f6f4 v[64:67], v[8:15], v[56:63], v[64:67], v252, v251 op_sel_hi:[0,0,0]
	s_setprio 0
	s_barrier
; #define PG8_STAGE(bufoff, gbase, voff) do { _Pragma("unroll") for (int _i = 0; _i < 2; ++_i) \
;         __builtin_amdgcn_global_load_lds((const unsigned*)((const char*)(gbase) + (voff)[_i]), (LAS unsigned*)(lds + (bufoff) + ldsw + _i * 8192), 16, 0, 0); } while (0)
; #define PG8_LDA(dst, b, h) do { _Pragma("unroll") for (int m = 0; m < 4; ++m) _Pragma("unroll") for (int k = 0; k < 2; ++k) dst[m][k] = *(const LAS bf16x8*)(lds + PG8_SA(b, h) + aoff + m * 2048 + k * KOFF); } while (0)
; #define PG8_LDB(dst, b, h) do { _Pragma("unroll") for (int n = 0; n < 2; ++n) _Pragma("unroll") for (int k = 0; k < 2; ++k) dst[n][k] = *(const LAS bf16x8*)(lds + PG8_SB(b, h) + boff + n * 2048 + k * KOFF); } while (0)
; #define PG8_WAIT_V(n) asm volatile("s_waitcnt vmcnt(" #n ")" ::: "memory")
; #define PG8_WAIT_L(n) asm volatile("s_waitcnt lgkmcnt(" #n ")" ::: "memory")
; #define PG8_BAR __builtin_amdgcn_s_barrier()
; #define PG8_SCHED __builtin_amdgcn_sched_barrier(0)
; template <class Epi, class Sched, bool GATHER, bool FP8 = false, bool ALIGN = true>
; __device__ __forceinline__ void gemm_phase(LAS unsigned char* lds, int wave, const Gemm g, const Sched& S, const Epi& E) {
;     ...
;             PG8_LDB(B0, 1, 0); PG8_LDB(B1, 1, 1); PG8_SCHED; PG8_LDA(At, 1, 0); PG8_STAGE(PG8_SA(0, 1), a2, ca1);
;             PG8_WAIT_V(8); PG8_WAIT_L(0); PG8_BAR; PG8_MMA(0, 0, At, B0); PG8_MMA(0, 1, At, B1); PG8_BAR; PG8_SCHED;
;             PG8_LDA(At, 1, 1); PG8_STAGE(PG8_SB(1, 0), b3, voffB0); PG8_STAGE(PG8_SB(1, 1), b3, voffB1); PG8_STAGE(PG8_SA(1, 0), a3, ca0);
;             PG8_WAIT_V(8); PG8_WAIT_L(0); PG8_BAR; PG8_MMA(1, 0, At, B0); PG8_MMA(1, 1, At, B1); PG8_BAR; PG8_SCHED;
	s_add_i32 s14, 0, 0x18000
	s_add_i32 s15, 0, 0x1c000
	v_add_u32_e32 v12, s14, v236
	v_add_u32_e32 v28, s15, v236
	ds_read_b128 v[0:3], v12
	ds_read_b128 v[4:7], v12 offset:1024
	ds_read_b128 v[8:11], v12 offset:2048
	ds_read_b128 v[12:15], v12 offset:3072
	ds_read_b128 v[16:19], v28
	ds_read_b128 v[20:23], v28 offset:1024
	ds_read_b128 v[24:27], v28 offset:2048
	ds_read_b128 v[28:31], v28 offset:3072
	s_mov_b32 m0, s56
	v_lshl_add_u64 v[230:231], s[12:13], 0, v[212:213]
	ds_read_b128 v[32:35], v238 offset:32768
	ds_read_b128 v[36:39], v238 offset:33792
	ds_read_b128 v[40:43], v238 offset:34816
	ds_read_b128 v[44:47], v238 offset:35840
	ds_read_b128 v[48:51], v238 offset:36864
	ds_read_b128 v[52:55], v238 offset:37888
	ds_read_b128 v[56:59], v238 offset:38912
	ds_read_b128 v[60:63], v238 offset:39936
	global_load_lds_dwordx4 v[230:231], off
	v_lshl_add_u64 v[230:231], s[12:13], 0, v[216:217]
	s_mov_b32 m0, s57
	s_nop 0
	global_load_lds_dwordx4 v[230:231], off
	s_waitcnt vmcnt(8)
	s_waitcnt lgkmcnt(0)
	s_barrier
	s_setprio 1
	s_waitcnt lgkmcnt(0)
	v_mfma_scale_f32_16x16x128_f8f6f4 v[188:191], v[0:7], v[32:39], v[188:191], v252, v251 op_sel_hi:[0,0,0]
	v_mfma_scale_f32_16x16x128_f8f6f4 v[180:183], v[8:15], v[32:39], v[180:183], v252, v251 op_sel_hi:[0,0,0]
	v_mfma_scale_f32_16x16x128_f8f6f4 v[172:175], v[0:7], v[40:47], v[172:175], v252, v251 op_sel_hi:[0,0,0]
	v_mfma_scale_f32_16x16x128_f8f6f4 v[164:167], v[8:15], v[40:47], v[164:167], v252, v251 op_sel_hi:[0,0,0]
	v_mfma_scale_f32_16x16x128_f8f6f4 v[156:159], v[0:7], v[48:55], v[156:159], v252, v251 op_sel_hi:[0,0,0]
	v_mfma_scale_f32_16x16x128_f8f6f4 v[148:151], v[8:15], v[48:55], v[148:151], v252, v251 op_sel_hi:[0,0,0]
	v_mfma_scale_f32_16x16x128_f8f6f4 v[140:143], v[0:7], v[56:63], v[140:143], v252, v251 op_sel_hi:[0,0,0]
	v_mfma_scale_f32_16x16x128_f8f6f4 v[132:135], v[8:15], v[56:63], v[132:135], v252, v251 op_sel_hi:[0,0,0]
	s_setprio 0
	s_setprio 1
	v_mfma_scale_f32_16x16x128_f8f6f4 v[184:187], v[16:23], v[32:39], v[184:187], v252, v251 op_sel_hi:[0,0,0]
	v_mfma_scale_f32_16x16x128_f8f6f4 v[176:179], v[24:31], v[32:39], v[176:179], v252, v251 op_sel_hi:[0,0,0]
	v_mfma_scale_f32_16x16x128_f8f6f4 v[168:171], v[16:23], v[40:47], v[168:171], v252, v251 op_sel_hi:[0,0,0]
	v_mfma_scale_f32_16x16x128_f8f6f4 v[160:163], v[24:31], v[40:47], v[160:163], v252, v251 op_sel_hi:[0,0,0]
	v_mfma_scale_f32_16x16x128_f8f6f4 v[152:155], v[16:23], v[48:55], v[152:155], v252, v251 op_sel_hi:[0,0,0]
	v_mfma_scale_f32_16x16x128_f8f6f4 v[144:147], v[24:31], v[48:55], v[144:147], v252, v251 op_sel_hi:[0,0,0]
	v_mfma_scale_f32_16x16x128_f8f6f4 v[136:139], v[16:23], v[56:63], v[136:139], v252, v251 op_sel_hi:[0,0,0]
	v_mfma_scale_f32_16x16x128_f8f6f4 v[128:131], v[24:31], v[56:63], v[128:131], v252, v251 op_sel_hi:[0,0,0]
	s_setprio 0
	s_barrier
	s_add_i32 s12, s14, s30
	v_lshl_add_u64 v[196:197], v[196:197], 0, s[62:63]
	s_mov_b32 m0, s12
	ds_read_b128 v[32:35], v238 offset:49152
	ds_read_b128 v[36:39], v238 offset:50176
	ds_read_b128 v[40:43], v238 offset:51200
	ds_read_b128 v[44:47], v238 offset:52224
	ds_read_b128 v[48:51], v238 offset:53248
	ds_read_b128 v[52:55], v238 offset:54272
	ds_read_b128 v[56:59], v238 offset:55296
	ds_read_b128 v[60:63], v238 offset:56320
	global_load_lds_dwordx4 v[196:197], off
	v_lshl_add_u64 v[196:197], v[198:199], 0, s[62:63]
	s_add_i32 m0, s12, 0x2000
	s_add_i32 s12, s15, s30
	global_load_lds_dwordx4 v[196:197], off
	v_lshl_add_u64 v[196:197], v[200:201], 0, s[62:63]
	s_mov_b32 m0, s12
	s_nop 0
	global_load_lds_dwordx4 v[196:197], off
	v_lshl_add_u64 v[196:197], v[202:203], 0, s[62:63]
	s_add_i32 m0, s12, 0x2000
	s_nop 0
	global_load_lds_dwordx4 v[196:197], off
	v_lshl_add_u64 v[196:197], v[226:227], 0, s[62:63]
	s_mov_b32 m0, s58
	s_nop 0
	global_load_lds_dwordx4 v[196:197], off
	v_lshl_add_u64 v[196:197], v[228:229], 0, s[62:63]
	s_mov_b32 m0, s59
	s_nop 0
	global_load_lds_dwordx4 v[196:197], off
	s_waitcnt vmcnt(8)
	s_waitcnt lgkmcnt(0)
	s_barrier
	s_setprio 1
	s_waitcnt lgkmcnt(0)
	v_mfma_scale_f32_16x16x128_f8f6f4 v[124:127], v[0:7], v[32:39], v[124:127], v252, v251 op_sel_hi:[0,0,0]
	v_mfma_scale_f32_16x16x128_f8f6f4 v[116:119], v[8:15], v[32:39], v[116:119], v252, v251 op_sel_hi:[0,0,0]
	v_mfma_scale_f32_16x16x128_f8f6f4 v[108:111], v[0:7], v[40:47], v[108:111], v252, v251 op_sel_hi:[0,0,0]
	v_mfma_scale_f32_16x16x128_f8f6f4 v[100:103], v[8:15], v[40:47], v[100:103], v252, v251 op_sel_hi:[0,0,0]
	v_mfma_scale_f32_16x16x128_f8f6f4 v[92:95], v[0:7], v[48:55], v[92:95], v252, v251 op_sel_hi:[0,0,0]
	v_mfma_scale_f32_16x16x128_f8f6f4 v[84:87], v[8:15], v[48:55], v[84:87], v252, v251 op_sel_hi:[0,0,0]
	v_mfma_scale_f32_16x16x128_f8f6f4 v[76:79], v[0:7], v[56:63], v[76:79], v252, v251 op_sel_hi:[0,0,0]
	v_mfma_scale_f32_16x16x128_f8f6f4 v[68:71], v[8:15], v[56:63], v[68:71], v252, v251 op_sel_hi:[0,0,0]
	s_setprio 0
	s_setprio 1
	v_mfma_scale_f32_16x16x128_f8f6f4 v[120:123], v[16:23], v[32:39], v[120:123], v252, v251 op_sel_hi:[0,0,0]
	v_mfma_scale_f32_16x16x128_f8f6f4 v[112:115], v[24:31], v[32:39], v[112:115], v252, v251 op_sel_hi:[0,0,0]
	v_mfma_scale_f32_16x16x128_f8f6f4 v[104:107], v[16:23], v[40:47], v[104:107], v252, v251 op_sel_hi:[0,0,0]
	v_mfma_scale_f32_16x16x128_f8f6f4 v[96:99], v[24:31], v[40:47], v[96:99], v252, v251 op_sel_hi:[0,0,0]
	v_mfma_scale_f32_16x16x128_f8f6f4 v[88:91], v[16:23], v[48:55], v[88:91], v252, v251 op_sel_hi:[0,0,0]
	v_mfma_scale_f32_16x16x128_f8f6f4 v[80:83], v[24:31], v[48:55], v[80:83], v252, v251 op_sel_hi:[0,0,0]
	v_mfma_scale_f32_16x16x128_f8f6f4 v[72:75], v[16:23], v[56:63], v[72:75], v252, v251 op_sel_hi:[0,0,0]
	v_mfma_scale_f32_16x16x128_f8f6f4 v[64:67], v[24:31], v[56:63], v[64:67], v252, v251 op_sel_hi:[0,0,0]
	s_setprio 0
	s_barrier
	s_add_i32 s83, s83, 2
	s_add_u32 s10, s10, 0x100
	s_addc_u32 s11, s11, 0
	s_add_u32 s49, s49, 0x100
	s_addc_u32 s82, s82, 0
	s_cmp_gt_u32 s83, 13
	s_cbranch_scc1 .LBB0_1083

; __device__ __forceinline__ unsigned pk4_fp8(float a, float b, float c, float d) { int w = __builtin_amdgcn_cvt_pk_fp8_f32(a, b, 0, false); w = __builtin_amdgcn_cvt_pk_fp8_f32(c, d, w, true); return (unsigned)w; }
; __device__ __forceinline__ float sigmoidf_(float x) { return __builtin_amdgcn_rcpf(1.0f + __expf(-x)); }
; __device__ __forceinline__ unsigned cvt_pk_bf16(float lo, float hi) { typedef __bf16 bf16x2_t __attribute__((ext_vector_type(2))); f32x2 v = {lo, hi}; bf16x2_t b = __builtin_convertvector(v, bf16x2_t); return __builtin_bit_cast(unsigned, b); }
;     __device__ __forceinline__ void operator()(const f32x4 (&acc)[2][2][4][2], const Unit& u, int wr, int wc, int fr, int fq) const {
;         const int row0 = u.pm * BM + wr * 64 + fr, col0 = u.pn * HALF + wc * 32 + 8 * fq;
; #pragma unroll
;         for (int ai = 0; ai < 2; ++ai)
; #pragma unroll
;             for (int m = 0; m < 4; ++m) { const size_t off = (size_t)(row0 + ai * HALF + m * 16) * DEXP + col0;
;                 float hv[8];
; #pragma unroll
;                 for (int n = 0; n < 2; ++n)
; #pragma unroll
;                     for (int j = 0; j < 4; ++j) { const float gg = acc[ai][0][m][n][j] * isc, uu = acc[ai][1][m][n][j] * isc; hv[4 * n + j] = gg * sigmoidf_(gg) * uu; }
;                 if constexpr (FP8OUT) { u32x2 w; w.x = pk4_fp8(hv[0], hv[1], hv[2], hv[3]); w.y = pk4_fp8(hv[4], hv[5], hv[6], hv[7]); *(u32x2*)((unsigned char*)H + off) = w; }
;                 else { u32x4 w; w.x = cvt_pk_bf16(hv[0], hv[1]); w.y = cvt_pk_bf16(hv[2], hv[3]); w.z = cvt_pk_bf16(hv[4], hv[5]); w.w = cvt_pk_bf16(hv[6], hv[7]); *(u32x4*)((bf16*)H + off) = w; } }
.LBB0_1085:
	v_lshl_add_u32 v10, s79, 8, v235
	v_ashrrev_i32_e32 v11, 31, v10
	v_lshl_add_u32 v14, s8, 7, v237
	v_ashrrev_i32_e32 v15, 31, v14
	s_mov_b64 s[8:9], -1
	v_lshlrev_b64 v[10:11], 9, v[10:11]
	v_lshl_add_u64 v[10:11], s[42:43], 0, v[10:11]
	v_lshl_add_u64 v[10:11], v[10:11], 0, v[14:15]
	v_mul_f32_e32 v0, 0xbfb8aa3b, v188
	v_mul_f32_e32 v1, 0xbfb8aa3b, v189
	v_mul_f32_e32 v2, 0xbfb8aa3b, v190
	v_mul_f32_e32 v3, 0xbfb8aa3b, v191
	v_mul_f32_e32 v4, 0xbfb8aa3b, v180
	v_mul_f32_e32 v5, 0xbfb8aa3b, v181
	v_mul_f32_e32 v6, 0xbfb8aa3b, v182
	v_mul_f32_e32 v7, 0xbfb8aa3b, v183
	v_exp_f32_e32 v0, v0
	v_exp_f32_e32 v1, v1
	v_exp_f32_e32 v2, v2
	v_exp_f32_e32 v3, v3
	v_exp_f32_e32 v4, v4
	v_exp_f32_e32 v5, v5
	v_exp_f32_e32 v6, v6
	v_exp_f32_e32 v7, v7
	v_add_f32_e32 v0, 1.0, v0
	v_add_f32_e32 v1, 1.0, v1
	v_add_f32_e32 v2, 1.0, v2
	v_add_f32_e32 v3, 1.0, v3
	v_add_f32_e32 v4, 1.0, v4
	v_add_f32_e32 v5, 1.0, v5
	v_add_f32_e32 v6, 1.0, v6
	v_add_f32_e32 v7, 1.0, v7
	v_rcp_f32_e32 v0, v0
	v_rcp_f32_e32 v1, v1
	v_rcp_f32_e32 v2, v2
	v_rcp_f32_e32 v3, v3
	v_rcp_f32_e32 v4, v4
	v_rcp_f32_e32 v5, v5
	v_rcp_f32_e32 v6, v6
	v_rcp_f32_e32 v7, v7
	v_mul_f32_e32 v0, v188, v0
	v_mul_f32_e32 v1, v189, v1
	v_mul_f32_e32 v2, v190, v2
	v_mul_f32_e32 v3, v191, v3
	v_mul_f32_e32 v4, v180, v4
	v_mul_f32_e32 v5, v181, v5
	v_mul_f32_e32 v6, v182, v6
	v_mul_f32_e32 v7, v183, v7
	v_mul_f32_e32 v0, v0, v184
	v_mul_f32_e32 v1, v1, v185
	v_mul_f32_e32 v2, v2, v186
	v_mul_f32_e32 v3, v3, v187
	v_mul_f32_e32 v4, v4, v176
	v_mul_f32_e32 v5, v5, v177
	v_mul_f32_e32 v6, v6, v178
	v_mul_f32_e32 v7, v7, v179
	v_cvt_pk_fp8_f32 v8, v0, v1
	v_cvt_pk_fp8_f32 v9, v4, v5
	v_cvt_pk_fp8_f32 v8, v2, v3 op_sel:[0,0,1]
	v_cvt_pk_fp8_f32 v9, v6, v7 op_sel:[0,0,1]
	global_store_dwordx2 v[10:11], v[8:9], off
	v_mul_f32_e32 v16, 0xbfb8aa3b, v172
	v_mul_f32_e32 v17, 0xbfb8aa3b, v173
	v_mul_f32_e32 v18, 0xbfb8aa3b, v174
	v_mul_f32_e32 v19, 0xbfb8aa3b, v175
	v_mul_f32_e32 v20, 0xbfb8aa3b, v164
	v_mul_f32_e32 v21, 0xbfb8aa3b, v165
	v_mul_f32_e32 v22, 0xbfb8aa3b, v166
	v_mul_f32_e32 v23, 0xbfb8aa3b, v167
	v_add_co_u32_e32 v28, vcc, 0x2000, v10
	v_exp_f32_e32 v16, v16
	v_exp_f32_e32 v17, v17
	v_exp_f32_e32 v18, v18
	v_exp_f32_e32 v19, v19
	v_exp_f32_e32 v20, v20
	v_exp_f32_e32 v21, v21
	v_exp_f32_e32 v22, v22
	v_exp_f32_e32 v23, v23
	v_addc_co_u32_e32 v29, vcc, 0, v11, vcc
	v_add_f32_e32 v16, 1.0, v16
	v_add_f32_e32 v17, 1.0, v17
	v_add_f32_e32 v18, 1.0, v18
	v_add_f32_e32 v19, 1.0, v19
	v_add_f32_e32 v20, 1.0, v20
	v_add_f32_e32 v21, 1.0, v21
	v_add_f32_e32 v22, 1.0, v22
	v_add_f32_e32 v23, 1.0, v23
	v_rcp_f32_e32 v16, v16
	v_rcp_f32_e32 v17, v17
	v_rcp_f32_e32 v18, v18
	v_rcp_f32_e32 v19, v19
	v_rcp_f32_e32 v20, v20
	v_rcp_f32_e32 v21, v21
	v_rcp_f32_e32 v22, v22
	v_rcp_f32_e32 v23, v23
	v_mul_f32_e32 v16, v172, v16
	v_mul_f32_e32 v17, v173, v17
	v_mul_f32_e32 v18, v174, v18
	v_mul_f32_e32 v19, v175, v19
	v_mul_f32_e32 v20, v164, v20
	v_mul_f32_e32 v21, v165, v21
	v_mul_f32_e32 v22, v166, v22
	v_mul_f32_e32 v23, v167, v23
	v_mul_f32_e32 v16, v16, v168
	v_mul_f32_e32 v17, v17, v169
	v_mul_f32_e32 v18, v18, v170
	v_mul_f32_e32 v19, v19, v171
	v_mul_f32_e32 v20, v20, v160
	v_mul_f32_e32 v21, v21, v161
	v_mul_f32_e32 v22, v22, v162
	v_mul_f32_e32 v23, v23, v163
	v_cvt_pk_fp8_f32 v24, v16, v17
	v_cvt_pk_fp8_f32 v25, v20, v21
	v_cvt_pk_fp8_f32 v24, v18, v19 op_sel:[0,0,1]
	v_cvt_pk_fp8_f32 v25, v22, v23 op_sel:[0,0,1]
	global_store_dwordx2 v[28:29], v[24:25], off
	v_mul_f32_e32 v0, 0xbfb8aa3b, v156
	v_mul_f32_e32 v1, 0xbfb8aa3b, v157
	v_mul_f32_e32 v2, 0xbfb8aa3b, v158
	v_mul_f32_e32 v3, 0xbfb8aa3b, v159
	v_mul_f32_e32 v4, 0xbfb8aa3b, v148
	v_mul_f32_e32 v5, 0xbfb8aa3b, v149
	v_mul_f32_e32 v6, 0xbfb8aa3b, v150
	v_mul_f32_e32 v7, 0xbfb8aa3b, v151
	v_add_co_u32_e32 v12, vcc, 0x4000, v10
	v_exp_f32_e32 v0, v0
	v_exp_f32_e32 v1, v1
	v_exp_f32_e32 v2, v2
	v_exp_f32_e32 v3, v3
	v_exp_f32_e32 v4, v4
	v_exp_f32_e32 v5, v5
	v_exp_f32_e32 v6, v6
	v_exp_f32_e32 v7, v7
	v_addc_co_u32_e32 v13, vcc, 0, v11, vcc
	v_add_f32_e32 v0, 1.0, v0
	v_add_f32_e32 v1, 1.0, v1
	v_add_f32_e32 v2, 1.0, v2
	v_add_f32_e32 v3, 1.0, v3
	v_add_f32_e32 v4, 1.0, v4
	v_add_f32_e32 v5, 1.0, v5
	v_add_f32_e32 v6, 1.0, v6
	v_add_f32_e32 v7, 1.0, v7
	v_rcp_f32_e32 v0, v0
	v_rcp_f32_e32 v1, v1
	v_rcp_f32_e32 v2, v2
	v_rcp_f32_e32 v3, v3
	v_rcp_f32_e32 v4, v4
	v_rcp_f32_e32 v5, v5
	v_rcp_f32_e32 v6, v6
	v_rcp_f32_e32 v7, v7
	v_mul_f32_e32 v0, v156, v0
	v_mul_f32_e32 v1, v157, v1
	v_mul_f32_e32 v2, v158, v2
	v_mul_f32_e32 v3, v159, v3
	v_mul_f32_e32 v4, v148, v4
	v_mul_f32_e32 v5, v149, v5
	v_mul_f32_e32 v6, v150, v6
	v_mul_f32_e32 v7, v151, v7
	v_mul_f32_e32 v0, v0, v152
	v_mul_f32_e32 v1, v1, v153
	v_mul_f32_e32 v2, v2, v154
	v_mul_f32_e32 v3, v3, v155
	v_mul_f32_e32 v4, v4, v144
	v_mul_f32_e32 v5, v5, v145
	v_mul_f32_e32 v6, v6, v146
	v_mul_f32_e32 v7, v7, v147
	v_cvt_pk_fp8_f32 v8, v0, v1
	v_cvt_pk_fp8_f32 v9, v4, v5
	v_cvt_pk_fp8_f32 v8, v2, v3 op_sel:[0,0,1]
	v_cvt_pk_fp8_f32 v9, v6, v7 op_sel:[0,0,1]
	global_store_dwordx2 v[12:13], v[8:9], off
	v_mul_f32_e32 v16, 0xbfb8aa3b, v140
	v_mul_f32_e32 v17, 0xbfb8aa3b, v141
	v_mul_f32_e32 v18, 0xbfb8aa3b, v142
	v_mul_f32_e32 v19, 0xbfb8aa3b, v143
	v_mul_f32_e32 v20, 0xbfb8aa3b, v132
	v_mul_f32_e32 v21, 0xbfb8aa3b, v133
	v_mul_f32_e32 v22, 0xbfb8aa3b, v134
	v_mul_f32_e32 v23, 0xbfb8aa3b, v135
	v_add_co_u32_e32 v28, vcc, 0x6000, v10
	v_exp_f32_e32 v16, v16
	v_exp_f32_e32 v17, v17
	v_exp_f32_e32 v18, v18
	v_exp_f32_e32 v19, v19
	v_exp_f32_e32 v20, v20
	v_exp_f32_e32 v21, v21
	v_exp_f32_e32 v22, v22
	v_exp_f32_e32 v23, v23
	v_addc_co_u32_e32 v29, vcc, 0, v11, vcc
	v_add_f32_e32 v16, 1.0, v16
; __device__ __forceinline__ unsigned pk4_fp8(float a, float b, float c, float d) { int w = __builtin_amdgcn_cvt_pk_fp8_f32(a, b, 0, false); w = __builtin_amdgcn_cvt_pk_fp8_f32(c, d, w, true); return (unsigned)w; }
; __device__ __forceinline__ float sigmoidf_(float x) { return __builtin_amdgcn_rcpf(1.0f + __expf(-x)); }
; __device__ __forceinline__ unsigned cvt_pk_bf16(float lo, float hi) { typedef __bf16 bf16x2_t __attribute__((ext_vector_type(2))); f32x2 v = {lo, hi}; bf16x2_t b = __builtin_convertvector(v, bf16x2_t); return __builtin_bit_cast(unsigned, b); }
;     __device__ __forceinline__ void operator()(const f32x4 (&acc)[2][2][4][2], const Unit& u, int wr, int wc, int fr, int fq) const {
;         const int row0 = u.pm * BM + wr * 64 + fr, col0 = u.pn * HALF + wc * 32 + 8 * fq;
; #pragma unroll
;         for (int ai = 0; ai < 2; ++ai)
; #pragma unroll
;             for (int m = 0; m < 4; ++m) { const size_t off = (size_t)(row0 + ai * HALF + m * 16) * DEXP + col0;
;                 float hv[8];
; #pragma unroll
;                 for (int n = 0; n < 2; ++n)
; #pragma unroll
;                     for (int j = 0; j < 4; ++j) { const float gg = acc[ai][0][m][n][j] * isc, uu = acc[ai][1][m][n][j] * isc; hv[4 * n + j] = gg * sigmoidf_(gg) * uu; }
;                 if constexpr (FP8OUT) { u32x2 w; w.x = pk4_fp8(hv[0], hv[1], hv[2], hv[3]); w.y = pk4_fp8(hv[4], hv[5], hv[6], hv[7]); *(u32x2*)((unsigned char*)H + off) = w; }
;                 else { u32x4 w; w.x = cvt_pk_bf16(hv[0], hv[1]); w.y = cvt_pk_bf16(hv[2], hv[3]); w.z = cvt_pk_bf16(hv[4], hv[5]); w.w = cvt_pk_bf16(hv[6], hv[7]); *(u32x4*)((bf16*)H + off) = w; } }
	v_add_f32_e32 v17, 1.0, v17
	v_add_f32_e32 v18, 1.0, v18
	v_add_f32_e32 v19, 1.0, v19
	v_add_f32_e32 v20, 1.0, v20
	v_add_f32_e32 v21, 1.0, v21
	v_add_f32_e32 v22, 1.0, v22
	v_add_f32_e32 v23, 1.0, v23
	v_rcp_f32_e32 v16, v16
	v_rcp_f32_e32 v17, v17
	v_rcp_f32_e32 v18, v18
	v_rcp_f32_e32 v19, v19
	v_rcp_f32_e32 v20, v20
	v_rcp_f32_e32 v21, v21
	v_rcp_f32_e32 v22, v22
	v_rcp_f32_e32 v23, v23
	v_mul_f32_e32 v16, v140, v16
	v_mul_f32_e32 v17, v141, v17
	v_mul_f32_e32 v18, v142, v18
	v_mul_f32_e32 v19, v143, v19
	v_mul_f32_e32 v20, v132, v20
	v_mul_f32_e32 v21, v133, v21
	v_mul_f32_e32 v22, v134, v22
	v_mul_f32_e32 v23, v135, v23
	v_mul_f32_e32 v16, v16, v136
	v_mul_f32_e32 v17, v17, v137
	v_mul_f32_e32 v18, v18, v138
	v_mul_f32_e32 v19, v19, v139
	v_mul_f32_e32 v20, v20, v128
	v_mul_f32_e32 v21, v21, v129
	v_mul_f32_e32 v22, v22, v130
	v_mul_f32_e32 v23, v23, v131
	v_cvt_pk_fp8_f32 v24, v16, v17
	v_cvt_pk_fp8_f32 v25, v20, v21
	v_cvt_pk_fp8_f32 v24, v18, v19 op_sel:[0,0,1]
	v_cvt_pk_fp8_f32 v25, v22, v23 op_sel:[0,0,1]
	global_store_dwordx2 v[28:29], v[24:25], off
	v_mul_f32_e32 v0, 0xbfb8aa3b, v124
	v_mul_f32_e32 v1, 0xbfb8aa3b, v125
	v_mul_f32_e32 v2, 0xbfb8aa3b, v126
	v_mul_f32_e32 v3, 0xbfb8aa3b, v127
	v_mul_f32_e32 v4, 0xbfb8aa3b, v116
	v_mul_f32_e32 v5, 0xbfb8aa3b, v117
	v_mul_f32_e32 v6, 0xbfb8aa3b, v118
	v_mul_f32_e32 v7, 0xbfb8aa3b, v119
	v_add_co_u32_e32 v12, vcc, 0x10000, v10
	v_exp_f32_e32 v0, v0
	v_exp_f32_e32 v1, v1
	v_exp_f32_e32 v2, v2
	v_exp_f32_e32 v3, v3
	v_exp_f32_e32 v4, v4
	v_exp_f32_e32 v5, v5
	v_exp_f32_e32 v6, v6
	v_exp_f32_e32 v7, v7
	v_addc_co_u32_e32 v13, vcc, 0, v11, vcc
	v_add_f32_e32 v0, 1.0, v0
	v_add_f32_e32 v1, 1.0, v1
	v_add_f32_e32 v2, 1.0, v2
	v_add_f32_e32 v3, 1.0, v3
	v_add_f32_e32 v4, 1.0, v4
	v_add_f32_e32 v5, 1.0, v5
	v_add_f32_e32 v6, 1.0, v6
	v_add_f32_e32 v7, 1.0, v7
	v_rcp_f32_e32 v0, v0
	v_rcp_f32_e32 v1, v1
	v_rcp_f32_e32 v2, v2
	v_rcp_f32_e32 v3, v3
	v_rcp_f32_e32 v4, v4
	v_rcp_f32_e32 v5, v5
	v_rcp_f32_e32 v6, v6
	v_rcp_f32_e32 v7, v7
	v_mul_f32_e32 v0, v124, v0
	v_mul_f32_e32 v1, v125, v1
	v_mul_f32_e32 v2, v126, v2
	v_mul_f32_e32 v3, v127, v3
	v_mul_f32_e32 v4, v116, v4
	v_mul_f32_e32 v5, v117, v5
	v_mul_f32_e32 v6, v118, v6
	v_mul_f32_e32 v7, v119, v7
	v_mul_f32_e32 v0, v0, v120
	v_mul_f32_e32 v1, v1, v121
	v_mul_f32_e32 v2, v2, v122
	v_mul_f32_e32 v3, v3, v123
	v_mul_f32_e32 v4, v4, v112
	v_mul_f32_e32 v5, v5, v113
	v_mul_f32_e32 v6, v6, v114
	v_mul_f32_e32 v7, v7, v115
	v_cvt_pk_fp8_f32 v8, v0, v1
	v_cvt_pk_fp8_f32 v9, v4, v5
	v_cvt_pk_fp8_f32 v8, v2, v3 op_sel:[0,0,1]
	v_cvt_pk_fp8_f32 v9, v6, v7 op_sel:[0,0,1]
	global_store_dwordx2 v[12:13], v[8:9], off
	v_mul_f32_e32 v16, 0xbfb8aa3b, v108
	v_mul_f32_e32 v17, 0xbfb8aa3b, v109
	v_mul_f32_e32 v18, 0xbfb8aa3b, v110
	v_mul_f32_e32 v19, 0xbfb8aa3b, v111
	v_mul_f32_e32 v20, 0xbfb8aa3b, v100
	v_mul_f32_e32 v21, 0xbfb8aa3b, v101
	v_mul_f32_e32 v22, 0xbfb8aa3b, v102
	v_mul_f32_e32 v23, 0xbfb8aa3b, v103
	v_add_co_u32_e32 v28, vcc, 0x12000, v10
	v_exp_f32_e32 v16, v16
	v_exp_f32_e32 v17, v17
	v_exp_f32_e32 v18, v18
	v_exp_f32_e32 v19, v19
	v_exp_f32_e32 v20, v20
	v_exp_f32_e32 v21, v21
	v_exp_f32_e32 v22, v22
	v_exp_f32_e32 v23, v23
	v_addc_co_u32_e32 v29, vcc, 0, v11, vcc
	v_add_f32_e32 v16, 1.0, v16
	v_add_f32_e32 v17, 1.0, v17
	v_add_f32_e32 v18, 1.0, v18
	v_add_f32_e32 v19, 1.0, v19
	v_add_f32_e32 v20, 1.0, v20
	v_add_f32_e32 v21, 1.0, v21
	v_add_f32_e32 v22, 1.0, v22
	v_add_f32_e32 v23, 1.0, v23
	v_rcp_f32_e32 v16, v16
	v_rcp_f32_e32 v17, v17
	v_rcp_f32_e32 v18, v18
	v_rcp_f32_e32 v19, v19
	v_rcp_f32_e32 v20, v20
	v_rcp_f32_e32 v21, v21
	v_rcp_f32_e32 v22, v22
	v_rcp_f32_e32 v23, v23
	v_mul_f32_e32 v16, v108, v16
	v_mul_f32_e32 v17, v109, v17
	v_mul_f32_e32 v18, v110, v18
	v_mul_f32_e32 v19, v111, v19
	v_mul_f32_e32 v20, v100, v20
	v_mul_f32_e32 v21, v101, v21
; __device__ __forceinline__ unsigned pk4_fp8(float a, float b, float c, float d) { int w = __builtin_amdgcn_cvt_pk_fp8_f32(a, b, 0, false); w = __builtin_amdgcn_cvt_pk_fp8_f32(c, d, w, true); return (unsigned)w; }
; __device__ __forceinline__ float sigmoidf_(float x) { return __builtin_amdgcn_rcpf(1.0f + __expf(-x)); }
; #define PG8_BAR __builtin_amdgcn_s_barrier()
; __device__ __forceinline__ unsigned cvt_pk_bf16(float lo, float hi) { typedef __bf16 bf16x2_t __attribute__((ext_vector_type(2))); f32x2 v = {lo, hi}; bf16x2_t b = __builtin_convertvector(v, bf16x2_t); return __builtin_bit_cast(unsigned, b); }
; template <class Epi, class Sched, bool GATHER, bool FP8 = false, bool ALIGN = true>
; __device__ __forceinline__ void gemm_phase(LAS unsigned char* lds, int wave, const Gemm g, const Sched& S, const Epi& E) {
;     ...
;         E(acc, cur, wr, wc, fr, fq);
;         if (!has_next) break;
; #pragma unroll
;         for (int a = 0; a < 2; ++a)
; #pragma unroll
;             for (int b = 0; b < 2; ++b)
; #pragma unroll
;                 for (int m = 0; m < 4; ++m)
; #pragma unroll
;                     for (int n = 0; n < 2; ++n) acc[a][b][m][n] = (f32x4){0.f, 0.f, 0.f, 0.f};
;         cur = nxt; cB = nB; ++ui;
;         if constexpr (ALIGN) { if (wr == 1) PG8_BAR; }
;     __device__ __forceinline__ void operator()(const f32x4 (&acc)[2][2][4][2], const Unit& u, int wr, int wc, int fr, int fq) const {
;         const int row0 = u.pm * BM + wr * 64 + fr, col0 = u.pn * HALF + wc * 32 + 8 * fq;
; #pragma unroll
;         for (int ai = 0; ai < 2; ++ai)
; #pragma unroll
;             for (int m = 0; m < 4; ++m) { const size_t off = (size_t)(row0 + ai * HALF + m * 16) * DEXP + col0;
;                 float hv[8];
; #pragma unroll
;                 for (int n = 0; n < 2; ++n)
; #pragma unroll
;                     for (int j = 0; j < 4; ++j) { const float gg = acc[ai][0][m][n][j] * isc, uu = acc[ai][1][m][n][j] * isc; hv[4 * n + j] = gg * sigmoidf_(gg) * uu; }
;                 if constexpr (FP8OUT) { u32x2 w; w.x = pk4_fp8(hv[0], hv[1], hv[2], hv[3]); w.y = pk4_fp8(hv[4], hv[5], hv[6], hv[7]); *(u32x2*)((unsigned char*)H + off) = w; }
;                 else { u32x4 w; w.x = cvt_pk_bf16(hv[0], hv[1]); w.y = cvt_pk_bf16(hv[2], hv[3]); w.z = cvt_pk_bf16(hv[4], hv[5]); w.w = cvt_pk_bf16(hv[6], hv[7]); *(u32x4*)((bf16*)H + off) = w; } }
	v_mul_f32_e32 v22, v102, v22
	v_mul_f32_e32 v23, v103, v23
	v_mul_f32_e32 v16, v16, v104
	v_mul_f32_e32 v17, v17, v105
	v_mul_f32_e32 v18, v18, v106
	v_mul_f32_e32 v19, v19, v107
	v_mul_f32_e32 v20, v20, v96
	v_mul_f32_e32 v21, v21, v97
	v_mul_f32_e32 v22, v22, v98
	v_mul_f32_e32 v23, v23, v99
	v_cvt_pk_fp8_f32 v24, v16, v17
	v_cvt_pk_fp8_f32 v25, v20, v21
	v_cvt_pk_fp8_f32 v24, v18, v19 op_sel:[0,0,1]
	v_cvt_pk_fp8_f32 v25, v22, v23 op_sel:[0,0,1]
	global_store_dwordx2 v[28:29], v[24:25], off
	v_mul_f32_e32 v0, 0xbfb8aa3b, v92
	v_mul_f32_e32 v1, 0xbfb8aa3b, v93
	v_mul_f32_e32 v2, 0xbfb8aa3b, v94
	v_mul_f32_e32 v3, 0xbfb8aa3b, v95
	v_mul_f32_e32 v4, 0xbfb8aa3b, v84
	v_mul_f32_e32 v5, 0xbfb8aa3b, v85
	v_mul_f32_e32 v6, 0xbfb8aa3b, v86
	v_mul_f32_e32 v7, 0xbfb8aa3b, v87
	v_add_co_u32_e32 v12, vcc, 0x14000, v10
	v_exp_f32_e32 v0, v0
	v_exp_f32_e32 v1, v1
	v_exp_f32_e32 v2, v2
	v_exp_f32_e32 v3, v3
	v_exp_f32_e32 v4, v4
	v_exp_f32_e32 v5, v5
	v_exp_f32_e32 v6, v6
	v_exp_f32_e32 v7, v7
	v_addc_co_u32_e32 v13, vcc, 0, v11, vcc
	v_add_f32_e32 v0, 1.0, v0
	v_add_f32_e32 v1, 1.0, v1
	v_add_f32_e32 v2, 1.0, v2
	v_add_f32_e32 v3, 1.0, v3
	v_add_f32_e32 v4, 1.0, v4
	v_add_f32_e32 v5, 1.0, v5
	v_add_f32_e32 v6, 1.0, v6
	v_add_f32_e32 v7, 1.0, v7
	v_rcp_f32_e32 v0, v0
	v_rcp_f32_e32 v1, v1
	v_rcp_f32_e32 v2, v2
	v_rcp_f32_e32 v3, v3
	v_rcp_f32_e32 v4, v4
	v_rcp_f32_e32 v5, v5
	v_rcp_f32_e32 v6, v6
	v_rcp_f32_e32 v7, v7
	v_mul_f32_e32 v0, v92, v0
	v_mul_f32_e32 v1, v93, v1
	v_mul_f32_e32 v2, v94, v2
	v_mul_f32_e32 v3, v95, v3
	v_mul_f32_e32 v4, v84, v4
	v_mul_f32_e32 v5, v85, v5
	v_mul_f32_e32 v6, v86, v6
	v_mul_f32_e32 v7, v87, v7
	v_mul_f32_e32 v0, v0, v88
	v_mul_f32_e32 v1, v1, v89
	v_mul_f32_e32 v2, v2, v90
	v_mul_f32_e32 v3, v3, v91
	v_mul_f32_e32 v4, v4, v80
	v_mul_f32_e32 v5, v5, v81
	v_mul_f32_e32 v6, v6, v82
	v_mul_f32_e32 v7, v7, v83
	v_cvt_pk_fp8_f32 v8, v0, v1
	v_cvt_pk_fp8_f32 v9, v4, v5
	v_cvt_pk_fp8_f32 v8, v2, v3 op_sel:[0,0,1]
	v_cvt_pk_fp8_f32 v9, v6, v7 op_sel:[0,0,1]
	global_store_dwordx2 v[12:13], v[8:9], off
	v_mul_f32_e32 v16, 0xbfb8aa3b, v76
	v_mul_f32_e32 v17, 0xbfb8aa3b, v77
	v_mul_f32_e32 v18, 0xbfb8aa3b, v78
	v_mul_f32_e32 v19, 0xbfb8aa3b, v79
	v_mul_f32_e32 v20, 0xbfb8aa3b, v68
	v_mul_f32_e32 v21, 0xbfb8aa3b, v69
	v_mul_f32_e32 v22, 0xbfb8aa3b, v70
	v_mul_f32_e32 v23, 0xbfb8aa3b, v71
	v_add_co_u32_e32 v28, vcc, 0x16000, v10
	v_exp_f32_e32 v16, v16
	v_exp_f32_e32 v17, v17
	v_exp_f32_e32 v18, v18
	v_exp_f32_e32 v19, v19
	v_exp_f32_e32 v20, v20
	v_exp_f32_e32 v21, v21
	v_exp_f32_e32 v22, v22
	v_exp_f32_e32 v23, v23
	v_addc_co_u32_e32 v29, vcc, 0, v11, vcc
	v_add_f32_e32 v16, 1.0, v16
	v_add_f32_e32 v17, 1.0, v17
	v_add_f32_e32 v18, 1.0, v18
	v_add_f32_e32 v19, 1.0, v19
	v_add_f32_e32 v20, 1.0, v20
	v_add_f32_e32 v21, 1.0, v21
	v_add_f32_e32 v22, 1.0, v22
	v_add_f32_e32 v23, 1.0, v23
	v_rcp_f32_e32 v16, v16
	v_rcp_f32_e32 v17, v17
	v_rcp_f32_e32 v18, v18
	v_rcp_f32_e32 v19, v19
	v_rcp_f32_e32 v20, v20
	v_rcp_f32_e32 v21, v21
	v_rcp_f32_e32 v22, v22
	v_rcp_f32_e32 v23, v23
	v_mul_f32_e32 v16, v76, v16
	v_mul_f32_e32 v17, v77, v17
	v_mul_f32_e32 v18, v78, v18
	v_mul_f32_e32 v19, v79, v19
	v_mul_f32_e32 v20, v68, v20
	v_mul_f32_e32 v21, v69, v21
	v_mul_f32_e32 v22, v70, v22
	v_mul_f32_e32 v23, v71, v23
	v_mul_f32_e32 v16, v16, v72
	v_mul_f32_e32 v17, v17, v73
	v_mul_f32_e32 v18, v18, v74
	v_mul_f32_e32 v19, v19, v75
	v_mul_f32_e32 v20, v20, v64
	v_mul_f32_e32 v21, v21, v65
	v_mul_f32_e32 v22, v22, v66
	v_mul_f32_e32 v23, v23, v67
	v_cvt_pk_fp8_f32 v24, v16, v17
	v_cvt_pk_fp8_f32 v25, v20, v21
	v_cvt_pk_fp8_f32 v24, v18, v19 op_sel:[0,0,1]
	v_cvt_pk_fp8_f32 v25, v22, v23 op_sel:[0,0,1]
	s_andn2_b64 vcc, exec, s[50:51]
	global_store_dwordx2 v[28:29], v[24:25], off
	s_cbranch_vccnz .LBB0_1073
	s_andn2_b64 vcc, exec, s[38:39]
	s_cbranch_vccnz .LBB0_1072
	s_barrier
	s_branch .LBB0_1072

; #define LAS __attribute__((address_space(3)))
; __device__ __forceinline__ int lane_id() { unsigned z = 0u; asm volatile("" : "+v"(z)); return (int)__builtin_amdgcn_mbcnt_hi(~0u, __builtin_amdgcn_mbcnt_lo(~0u, z)); }
; #define REP(j) for (int rep_ = 0; rep_ < 1 + (((REPMASK) >> (j)) & 1); ++rep_)
; __global__ void __launch_bounds__(NTHR, 2) fwd(Args args) {
;     ...
;         if (EN(8) && IN(pb + 8)) {
;             PHASE_ENV();
;             LAS int* tp = (LAS int*)(Fp.lds + LDS_MISC - 512);
;             { int t_ = Fp.wave * 64 + lane_id(); asm volatile("" : "+v"(t_)); if (t_ < 66) tp[t_] = ETAB_[t_]; }
;             __syncthreads();
;             if (DOWN_FP8 && l >= FP8_FIRST) {
;                 gm::Gemm g{HB_, ws + WS_WDN + (size_t)l * NE1 * D * DEXP * 2, DEXP, nullptr, (size_t)D * DEXP};
;                 gm::GroupOrder S{tp, 8, Fp.G, Fp.vcu, 0};
;                 gm::EpiStore<true> E{YS_, D, YS8SCALE / W8SCALE};
;                 REP(8) { S.ecur = 0; gm::gemm_phase<gm::EpiStore<true>, gm::GroupOrder, false, true>(Fp.lds, Fp.wave, g, S, E); }
.LBB0_1139:
	s_andn2_b64 vcc, exec, s[4:5]
	s_cbranch_vccnz .LBB0_1214
	v_mov_b32_e32 v251, 0x7e7e7e7e
	v_readlane_b32 s4, v255, 8
	v_readlane_b32 s5, v255, 9
	v_readlane_b32 s12, v255, 7
	v_readlane_b32 s2, v255, 2
	v_readlane_b32 s22, v255, 4
	s_waitcnt vmcnt(0)
	v_mov_b32_e32 v0, v193
	s_load_dwordx2 s[36:37], s[4:5], 0x118
	s_movk_i32 s4, 0x42
	v_mbcnt_lo_u32_b32 v0, -1, v0
	v_mbcnt_hi_u32_b32 v0, -1, v0
	v_lshl_add_u32 v0, s12, 6, v0
	s_nop 0
	v_cmp_gt_i32_e32 vcc, s4, v0
	s_and_saveexec_b64 s[4:5], vcc
	s_cbranch_execz .LBB0_1142
	v_lshl_add_u32 v1, v0, 2, 0
	v_add_u32_e32 v2, 0x23d00, v1
	v_ashrrev_i32_e32 v1, 31, v0
	s_waitcnt lgkmcnt(0)
	v_lshl_add_u64 v[0:1], v[0:1], 2, s[36:37]
	v_add_co_u32_e32 v0, vcc, 0x100000, v0
	s_nop 1
	v_addc_co_u32_e32 v1, vcc, 0, v1, vcc
	global_load_dword v0, v[0:1], off
	s_waitcnt vmcnt(0)
	ds_write_b32 v2, v0

; #define PG8_STAGE(bufoff, gbase, voff) do { _Pragma("unroll") for (int _i = 0; _i < 2; ++_i) \
;         __builtin_amdgcn_global_load_lds((const unsigned*)((const char*)(gbase) + (voff)[_i]), (LAS unsigned*)(lds + (bufoff) + ldsw + _i * 8192), 16, 0, 0); } while (0)
; #define PG8_LDA(dst, b, h) do { _Pragma("unroll") for (int m = 0; m < 4; ++m) _Pragma("unroll") for (int k = 0; k < 2; ++k) dst[m][k] = *(const LAS bf16x8*)(lds + PG8_SA(b, h) + aoff + m * 2048 + k * KOFF); } while (0)
; #define PG8_LDB(dst, b, h) do { _Pragma("unroll") for (int n = 0; n < 2; ++n) _Pragma("unroll") for (int k = 0; k < 2; ++k) dst[n][k] = *(const LAS bf16x8*)(lds + PG8_SB(b, h) + boff + n * 2048 + k * KOFF); } while (0)
; #define PG8_WAIT_V(n) asm volatile("s_waitcnt vmcnt(" #n ")" ::: "memory")
; #define PG8_WAIT_L(n) asm volatile("s_waitcnt lgkmcnt(" #n ")" ::: "memory")
; #define PG8_BAR __builtin_amdgcn_s_barrier()
; #define PG8_SCHED __builtin_amdgcn_sched_barrier(0)
; #define PG8_AOFF(u_, o0, o1) do { _Pragma("unroll") for (int _i = 0; _i < 2; ++_i) { const int r0 = (u_).pm * BM + Rr[_i], r1 = r0 + HALF; \
;         const int g0 = GATHER ? g.rowidx[r0] : r0, g1 = GATHER ? g.rowidx[r1] : r1; \
;         o0[_i] = (unsigned)g0 * (unsigned)K + (unsigned)Cc[_i]; o1[_i] = (unsigned)g1 * (unsigned)K + (unsigned)Cc[_i]; } } while (0)
; template <class Epi, class Sched, bool GATHER, bool FP8 = false, bool ALIGN = true>
; __device__ __forceinline__ void gemm_phase(LAS unsigned char* lds, int wave, const Gemm g, const Sched& S, const Epi& E) {
;     ...
;             PG8_LDB(B0, 0, 0); PG8_LDB(B1, 0, 1); PG8_SCHED; PG8_LDA(At, 0, 0); PG8_STAGE(PG8_SA(1, 1), a1, ca1);
;             if (last && has_next) PG8_AOFF(nxt, ca0, ca1);
;             PG8_WAIT_V(8); PG8_WAIT_L(0); PG8_BAR; PG8_MMA(0, 0, At, B0); PG8_MMA(0, 1, At, B1); PG8_BAR; PG8_SCHED;
;             PG8_LDA(At, 0, 1); PG8_STAGE(PG8_SB(0, 0), b2, voffB0); PG8_STAGE(PG8_SB(0, 1), b2, voffB1); PG8_STAGE(PG8_SA(0, 0), a2, ca0);
;             PG8_WAIT_V(8); PG8_WAIT_L(0); PG8_BAR; PG8_MMA(1, 0, At, B0); PG8_MMA(1, 1, At, B1); PG8_BAR; PG8_SCHED;
.LBB0_1158:
	s_xor_b64 s[50:51], s[84:85], -1
	s_add_u32 s14, s12, 0x100
	s_addc_u32 s15, s13, 0
	s_and_b64 s[12:13], s[80:81], exec
	s_cselect_b32 s13, s7, s15
	s_cselect_b32 s12, s6, s14
	s_add_u32 s14, s48, s82
	s_addc_u32 s15, s49, s83
	s_waitcnt vmcnt(8)
	s_add_u32 s79, s14, 0x100
	s_waitcnt lgkmcnt(0)
	s_addc_u32 s82, s15, 0
	s_and_b64 s[14:15], s[80:81], exec
	s_cselect_b32 s15, s5, s82
	s_cselect_b32 s14, s39, s79
	s_barrier
	s_setprio 1
	s_waitcnt lgkmcnt(0)
	v_mfma_scale_f32_16x16x128_f8f6f4 v[188:191], v[16:23], v[56:63], v[188:191], v252, v251 op_sel_hi:[0,0,0]
	v_mfma_scale_f32_16x16x128_f8f6f4 v[184:187], v[24:31], v[56:63], v[184:187], v252, v251 op_sel_hi:[0,0,0]
	v_mfma_scale_f32_16x16x128_f8f6f4 v[172:175], v[16:23], v[48:55], v[172:175], v252, v251 op_sel_hi:[0,0,0]
	v_mfma_scale_f32_16x16x128_f8f6f4 v[168:171], v[24:31], v[48:55], v[168:171], v252, v251 op_sel_hi:[0,0,0]
	v_mfma_scale_f32_16x16x128_f8f6f4 v[156:159], v[16:23], v[40:47], v[156:159], v252, v251 op_sel_hi:[0,0,0]
	v_mfma_scale_f32_16x16x128_f8f6f4 v[152:155], v[24:31], v[40:47], v[152:155], v252, v251 op_sel_hi:[0,0,0]
	v_mfma_scale_f32_16x16x128_f8f6f4 v[140:143], v[16:23], v[32:39], v[140:143], v252, v251 op_sel_hi:[0,0,0]
	v_mfma_scale_f32_16x16x128_f8f6f4 v[136:139], v[24:31], v[32:39], v[136:139], v252, v251 op_sel_hi:[0,0,0]
	s_setprio 0
	s_setprio 1
	v_mfma_scale_f32_16x16x128_f8f6f4 v[180:183], v[0:7], v[56:63], v[180:183], v252, v251 op_sel_hi:[0,0,0]
	v_mfma_scale_f32_16x16x128_f8f6f4 v[176:179], v[8:15], v[56:63], v[176:179], v252, v251 op_sel_hi:[0,0,0]
	v_mfma_scale_f32_16x16x128_f8f6f4 v[164:167], v[0:7], v[48:55], v[164:167], v252, v251 op_sel_hi:[0,0,0]
	v_mfma_scale_f32_16x16x128_f8f6f4 v[160:163], v[8:15], v[48:55], v[160:163], v252, v251 op_sel_hi:[0,0,0]
	v_mfma_scale_f32_16x16x128_f8f6f4 v[148:151], v[0:7], v[40:47], v[148:151], v252, v251 op_sel_hi:[0,0,0]
	v_mfma_scale_f32_16x16x128_f8f6f4 v[144:147], v[8:15], v[40:47], v[144:147], v252, v251 op_sel_hi:[0,0,0]
	v_mfma_scale_f32_16x16x128_f8f6f4 v[132:135], v[0:7], v[32:39], v[132:135], v252, v251 op_sel_hi:[0,0,0]
	v_mfma_scale_f32_16x16x128_f8f6f4 v[128:131], v[8:15], v[32:39], v[128:131], v252, v251 op_sel_hi:[0,0,0]
	s_setprio 0
	s_barrier
	s_mov_b32 m0, s34
	v_lshl_add_u64 v[196:197], s[14:15], 0, v[204:205]
	ds_read_b128 v[32:35], v240 offset:16384
	ds_read_b128 v[36:39], v240 offset:17408
	ds_read_b128 v[40:43], v240 offset:18432
	ds_read_b128 v[44:47], v240 offset:19456
	ds_read_b128 v[48:51], v240 offset:20480
	ds_read_b128 v[52:55], v240 offset:21504
	ds_read_b128 v[56:59], v240 offset:22528
	ds_read_b128 v[60:63], v240 offset:23552
	global_load_lds_dwordx4 v[196:197], off
	v_lshl_add_u64 v[198:199], s[14:15], 0, v[208:209]
	s_mov_b32 m0, s35
	v_lshl_add_u64 v[200:201], s[14:15], 0, v[206:207]
	global_load_lds_dwordx4 v[198:199], off
	s_mov_b32 m0, s40
	v_lshl_add_u64 v[202:203], s[14:15], 0, v[210:211]
	global_load_lds_dwordx4 v[200:201], off
	s_mov_b32 m0, s41
	v_mov_b32_e32 v213, v193
	global_load_lds_dwordx4 v[202:203], off
	s_mov_b32 m0, s31
	v_mov_b32_e32 v215, v193
	global_load_lds_dwordx4 v212, s[12:13]
	s_mov_b32 m0, s47
	v_lshl_add_u64 v[226:227], s[12:13], 0, v[212:213]
	global_load_lds_dwordx4 v214, s[12:13]
	s_waitcnt vmcnt(8)
	s_waitcnt lgkmcnt(0)
	v_lshl_add_u64 v[228:229], s[12:13], 0, v[214:215]
	s_barrier
	s_setprio 1
	s_waitcnt lgkmcnt(0)
	v_mfma_scale_f32_16x16x128_f8f6f4 v[124:127], v[16:23], v[32:39], v[124:127], v252, v251 op_sel_hi:[0,0,0]
	v_mfma_scale_f32_16x16x128_f8f6f4 v[120:123], v[24:31], v[32:39], v[120:123], v252, v251 op_sel_hi:[0,0,0]
	v_mfma_scale_f32_16x16x128_f8f6f4 v[108:111], v[16:23], v[40:47], v[108:111], v252, v251 op_sel_hi:[0,0,0]
	v_mfma_scale_f32_16x16x128_f8f6f4 v[104:107], v[24:31], v[40:47], v[104:107], v252, v251 op_sel_hi:[0,0,0]
	v_mfma_scale_f32_16x16x128_f8f6f4 v[92:95], v[16:23], v[48:55], v[92:95], v252, v251 op_sel_hi:[0,0,0]
	v_mfma_scale_f32_16x16x128_f8f6f4 v[88:91], v[24:31], v[48:55], v[88:91], v252, v251 op_sel_hi:[0,0,0]
	v_mfma_scale_f32_16x16x128_f8f6f4 v[76:79], v[16:23], v[56:63], v[76:79], v252, v251 op_sel_hi:[0,0,0]
	v_mfma_scale_f32_16x16x128_f8f6f4 v[72:75], v[24:31], v[56:63], v[72:75], v252, v251 op_sel_hi:[0,0,0]
	s_setprio 0
	s_setprio 1
	v_mfma_scale_f32_16x16x128_f8f6f4 v[116:119], v[0:7], v[32:39], v[116:119], v252, v251 op_sel_hi:[0,0,0]
	v_mfma_scale_f32_16x16x128_f8f6f4 v[112:115], v[8:15], v[32:39], v[112:115], v252, v251 op_sel_hi:[0,0,0]
	v_mfma_scale_f32_16x16x128_f8f6f4 v[100:103], v[0:7], v[40:47], v[100:103], v252, v251 op_sel_hi:[0,0,0]
	v_mfma_scale_f32_16x16x128_f8f6f4 v[96:99], v[8:15], v[40:47], v[96:99], v252, v251 op_sel_hi:[0,0,0]
	v_mfma_scale_f32_16x16x128_f8f6f4 v[84:87], v[0:7], v[48:55], v[84:87], v252, v251 op_sel_hi:[0,0,0]
	v_mfma_scale_f32_16x16x128_f8f6f4 v[80:83], v[8:15], v[48:55], v[80:83], v252, v251 op_sel_hi:[0,0,0]
	v_mfma_scale_f32_16x16x128_f8f6f4 v[68:71], v[0:7], v[56:63], v[68:71], v252, v251 op_sel_hi:[0,0,0]
	v_mfma_scale_f32_16x16x128_f8f6f4 v[64:67], v[8:15], v[56:63], v[64:67], v252, v251 op_sel_hi:[0,0,0]
	s_setprio 0
	s_barrier
; #define PG8_STAGE(bufoff, gbase, voff) do { _Pragma("unroll") for (int _i = 0; _i < 2; ++_i) \
;         __builtin_amdgcn_global_load_lds((const unsigned*)((const char*)(gbase) + (voff)[_i]), (LAS unsigned*)(lds + (bufoff) + ldsw + _i * 8192), 16, 0, 0); } while (0)
; #define PG8_LDA(dst, b, h) do { _Pragma("unroll") for (int m = 0; m < 4; ++m) _Pragma("unroll") for (int k = 0; k < 2; ++k) dst[m][k] = *(const LAS bf16x8*)(lds + PG8_SA(b, h) + aoff + m * 2048 + k * KOFF); } while (0)
; #define PG8_LDB(dst, b, h) do { _Pragma("unroll") for (int n = 0; n < 2; ++n) _Pragma("unroll") for (int k = 0; k < 2; ++k) dst[n][k] = *(const LAS bf16x8*)(lds + PG8_SB(b, h) + boff + n * 2048 + k * KOFF); } while (0)
; #define PG8_WAIT_V(n) asm volatile("s_waitcnt vmcnt(" #n ")" ::: "memory")
; #define PG8_WAIT_L(n) asm volatile("s_waitcnt lgkmcnt(" #n ")" ::: "memory")
; #define PG8_BAR __builtin_amdgcn_s_barrier()
; #define PG8_SCHED __builtin_amdgcn_sched_barrier(0)
; template <class Epi, class Sched, bool GATHER, bool FP8 = false, bool ALIGN = true>
; __device__ __forceinline__ void gemm_phase(LAS unsigned char* lds, int wave, const Gemm g, const Sched& S, const Epi& E) {
;     ...
;             PG8_LDB(B0, 1, 0); PG8_LDB(B1, 1, 1); PG8_SCHED; PG8_LDA(At, 1, 0); PG8_STAGE(PG8_SA(0, 1), a2, ca1);
;             PG8_WAIT_V(8); PG8_WAIT_L(0); PG8_BAR; PG8_MMA(0, 0, At, B0); PG8_MMA(0, 1, At, B1); PG8_BAR; PG8_SCHED;
;             PG8_LDA(At, 1, 1); PG8_STAGE(PG8_SB(1, 0), b3, voffB0); PG8_STAGE(PG8_SB(1, 1), b3, voffB1); PG8_STAGE(PG8_SA(1, 0), a3, ca0);
;             PG8_WAIT_V(8); PG8_WAIT_L(0); PG8_BAR; PG8_MMA(1, 0, At, B0); PG8_MMA(1, 1, At, B1); PG8_BAR; PG8_SCHED;
	s_add_i32 s14, 0, 0x18000
	s_add_i32 s15, 0, 0x1c000
	v_add_u32_e32 v12, s14, v236
	v_add_u32_e32 v28, s15, v236
	ds_read_b128 v[0:3], v12
	ds_read_b128 v[4:7], v12 offset:1024
	ds_read_b128 v[8:11], v12 offset:2048
	ds_read_b128 v[12:15], v12 offset:3072
	ds_read_b128 v[16:19], v28
	ds_read_b128 v[20:23], v28 offset:1024
	ds_read_b128 v[24:27], v28 offset:2048
	ds_read_b128 v[28:31], v28 offset:3072
	s_mov_b32 m0, s53
	v_lshl_add_u64 v[224:225], s[12:13], 0, v[224:225]
	ds_read_b128 v[32:35], v240 offset:32768
	ds_read_b128 v[36:39], v240 offset:33792
	ds_read_b128 v[40:43], v240 offset:34816
	ds_read_b128 v[44:47], v240 offset:35840
	ds_read_b128 v[48:51], v240 offset:36864
	ds_read_b128 v[52:55], v240 offset:37888
	ds_read_b128 v[56:59], v240 offset:38912
	ds_read_b128 v[60:63], v240 offset:39936
	global_load_lds_dwordx4 v[224:225], off
	v_lshl_add_u64 v[222:223], s[12:13], 0, v[222:223]
	s_mov_b32 m0, s56
	s_nop 0
	global_load_lds_dwordx4 v[222:223], off
	s_waitcnt vmcnt(8)
	s_waitcnt lgkmcnt(0)
	s_barrier
	s_setprio 1
	s_waitcnt lgkmcnt(0)
	v_mfma_scale_f32_16x16x128_f8f6f4 v[188:191], v[0:7], v[32:39], v[188:191], v252, v251 op_sel_hi:[0,0,0]
	v_mfma_scale_f32_16x16x128_f8f6f4 v[184:187], v[8:15], v[32:39], v[184:187], v252, v251 op_sel_hi:[0,0,0]
	v_mfma_scale_f32_16x16x128_f8f6f4 v[172:175], v[0:7], v[40:47], v[172:175], v252, v251 op_sel_hi:[0,0,0]
	v_mfma_scale_f32_16x16x128_f8f6f4 v[168:171], v[8:15], v[40:47], v[168:171], v252, v251 op_sel_hi:[0,0,0]
	v_mfma_scale_f32_16x16x128_f8f6f4 v[156:159], v[0:7], v[48:55], v[156:159], v252, v251 op_sel_hi:[0,0,0]
	v_mfma_scale_f32_16x16x128_f8f6f4 v[152:155], v[8:15], v[48:55], v[152:155], v252, v251 op_sel_hi:[0,0,0]
	v_mfma_scale_f32_16x16x128_f8f6f4 v[140:143], v[0:7], v[56:63], v[140:143], v252, v251 op_sel_hi:[0,0,0]
	v_mfma_scale_f32_16x16x128_f8f6f4 v[136:139], v[8:15], v[56:63], v[136:139], v252, v251 op_sel_hi:[0,0,0]
	s_setprio 0
	s_setprio 1
	v_mfma_scale_f32_16x16x128_f8f6f4 v[180:183], v[16:23], v[32:39], v[180:183], v252, v251 op_sel_hi:[0,0,0]
	v_mfma_scale_f32_16x16x128_f8f6f4 v[176:179], v[24:31], v[32:39], v[176:179], v252, v251 op_sel_hi:[0,0,0]
	v_mfma_scale_f32_16x16x128_f8f6f4 v[164:167], v[16:23], v[40:47], v[164:167], v252, v251 op_sel_hi:[0,0,0]
	v_mfma_scale_f32_16x16x128_f8f6f4 v[160:163], v[24:31], v[40:47], v[160:163], v252, v251 op_sel_hi:[0,0,0]
	v_mfma_scale_f32_16x16x128_f8f6f4 v[148:151], v[16:23], v[48:55], v[148:151], v252, v251 op_sel_hi:[0,0,0]
	v_mfma_scale_f32_16x16x128_f8f6f4 v[144:147], v[24:31], v[48:55], v[144:147], v252, v251 op_sel_hi:[0,0,0]
	v_mfma_scale_f32_16x16x128_f8f6f4 v[132:135], v[16:23], v[56:63], v[132:135], v252, v251 op_sel_hi:[0,0,0]
	v_mfma_scale_f32_16x16x128_f8f6f4 v[128:131], v[24:31], v[56:63], v[128:131], v252, v251 op_sel_hi:[0,0,0]
	s_setprio 0
	s_barrier
	s_add_i32 s12, s14, s30
	v_lshl_add_u64 v[196:197], v[196:197], 0, s[62:63]
	s_mov_b32 m0, s12
	ds_read_b128 v[32:35], v240 offset:49152
	ds_read_b128 v[36:39], v240 offset:50176
	ds_read_b128 v[40:43], v240 offset:51200
	ds_read_b128 v[44:47], v240 offset:52224
	ds_read_b128 v[48:51], v240 offset:53248
	ds_read_b128 v[52:55], v240 offset:54272
	ds_read_b128 v[56:59], v240 offset:55296
	ds_read_b128 v[60:63], v240 offset:56320
	global_load_lds_dwordx4 v[196:197], off
	v_lshl_add_u64 v[196:197], v[198:199], 0, s[62:63]
	s_add_i32 m0, s12, 0x2000
	s_add_i32 s12, s15, s30
	global_load_lds_dwordx4 v[196:197], off
	v_lshl_add_u64 v[196:197], v[200:201], 0, s[62:63]
	s_mov_b32 m0, s12
	s_nop 0
	global_load_lds_dwordx4 v[196:197], off
	v_lshl_add_u64 v[196:197], v[202:203], 0, s[62:63]
	s_add_i32 m0, s12, 0x2000
	s_nop 0
	global_load_lds_dwordx4 v[196:197], off
	v_lshl_add_u64 v[196:197], v[226:227], 0, s[62:63]
	s_mov_b32 m0, s57
	s_nop 0
	global_load_lds_dwordx4 v[196:197], off
	v_lshl_add_u64 v[196:197], v[228:229], 0, s[62:63]
	s_mov_b32 m0, s58
	s_nop 0
	global_load_lds_dwordx4 v[196:197], off
	s_waitcnt vmcnt(8)
	s_waitcnt lgkmcnt(0)
	s_barrier
	s_setprio 1
	s_waitcnt lgkmcnt(0)
	v_mfma_scale_f32_16x16x128_f8f6f4 v[124:127], v[0:7], v[32:39], v[124:127], v252, v251 op_sel_hi:[0,0,0]
	v_mfma_scale_f32_16x16x128_f8f6f4 v[120:123], v[8:15], v[32:39], v[120:123], v252, v251 op_sel_hi:[0,0,0]
	v_mfma_scale_f32_16x16x128_f8f6f4 v[108:111], v[0:7], v[40:47], v[108:111], v252, v251 op_sel_hi:[0,0,0]
	v_mfma_scale_f32_16x16x128_f8f6f4 v[104:107], v[8:15], v[40:47], v[104:107], v252, v251 op_sel_hi:[0,0,0]
	v_mfma_scale_f32_16x16x128_f8f6f4 v[92:95], v[0:7], v[48:55], v[92:95], v252, v251 op_sel_hi:[0,0,0]
	v_mfma_scale_f32_16x16x128_f8f6f4 v[88:91], v[8:15], v[48:55], v[88:91], v252, v251 op_sel_hi:[0,0,0]
	v_mfma_scale_f32_16x16x128_f8f6f4 v[76:79], v[0:7], v[56:63], v[76:79], v252, v251 op_sel_hi:[0,0,0]
	v_mfma_scale_f32_16x16x128_f8f6f4 v[72:75], v[8:15], v[56:63], v[72:75], v252, v251 op_sel_hi:[0,0,0]
	s_setprio 0
	s_setprio 1
	v_mfma_scale_f32_16x16x128_f8f6f4 v[116:119], v[16:23], v[32:39], v[116:119], v252, v251 op_sel_hi:[0,0,0]
	v_mfma_scale_f32_16x16x128_f8f6f4 v[112:115], v[24:31], v[32:39], v[112:115], v252, v251 op_sel_hi:[0,0,0]
	v_mfma_scale_f32_16x16x128_f8f6f4 v[100:103], v[16:23], v[40:47], v[100:103], v252, v251 op_sel_hi:[0,0,0]
	v_mfma_scale_f32_16x16x128_f8f6f4 v[96:99], v[24:31], v[40:47], v[96:99], v252, v251 op_sel_hi:[0,0,0]
	v_mfma_scale_f32_16x16x128_f8f6f4 v[84:87], v[16:23], v[48:55], v[84:87], v252, v251 op_sel_hi:[0,0,0]
	v_mfma_scale_f32_16x16x128_f8f6f4 v[80:83], v[24:31], v[48:55], v[80:83], v252, v251 op_sel_hi:[0,0,0]
	v_mfma_scale_f32_16x16x128_f8f6f4 v[68:71], v[16:23], v[56:63], v[68:71], v252, v251 op_sel_hi:[0,0,0]
	v_mfma_scale_f32_16x16x128_f8f6f4 v[64:67], v[24:31], v[56:63], v[64:67], v252, v251 op_sel_hi:[0,0,0]
	s_setprio 0
	s_barrier
	s_mov_b64 s[84:85], 0
	s_mov_b64 s[80:81], -1
	s_and_b64 vcc, exec, s[50:51]
	s_cbranch_vccnz .LBB0_1160
	s_mov_b64 s[82:83], 0x100
	s_branch .LBB0_1155

; __device__ __forceinline__ unsigned pk4_fp8(float a, float b, float c, float d) { int w = __builtin_amdgcn_cvt_pk_fp8_f32(a, b, 0, false); w = __builtin_amdgcn_cvt_pk_fp8_f32(c, d, w, true); return (unsigned)w; }
;     __device__ __forceinline__ void operator()(const f32x4 (&acc)[2][2][4][2], const Unit& u, int wr, int wc, int fr, int fq) const {
;         const int row0 = u.pm * BM + wr * 64 + fr, col0 = u.pn * BM + wc * 64 + 16 * fq;
; #pragma unroll
;         for (int ai = 0; ai < 2; ++ai)
; #pragma unroll
;             for (int m = 0; m < 4; ++m) { const size_t off = (size_t)(row0 + ai * HALF + m * 16) * ldc + col0;
;                 const f32x4 v0 = acc[ai][0][m][0] * scale, v1 = acc[ai][0][m][1] * scale, v2 = acc[ai][1][m][0] * scale, v3 = acc[ai][1][m][1] * scale;
;                 if constexpr (FP8OUT) { u32x4 w; w.x = pk4_fp8(v0[0], v0[1], v0[2], v0[3]); w.y = pk4_fp8(v1[0], v1[1], v1[2], v1[3]); w.z = pk4_fp8(v2[0], v2[1], v2[2], v2[3]); w.w = pk4_fp8(v3[0], v3[1], v3[2], v3[3]);
;                     *(u32x4*)((unsigned char*)O + off) = w; }
.LBB0_1162:
	v_cvt_pk_fp8_f32 v2, v188, v189
	v_cvt_pk_fp8_f32 v3, v184, v185
	v_cvt_pk_fp8_f32 v4, v180, v181
	v_cvt_pk_fp8_f32 v5, v176, v177
	v_lshl_add_u32 v6, s73, 8, v235
	v_ashrrev_i32_e32 v7, 31, v6
	v_cvt_pk_fp8_f32 v2, v190, v191 op_sel:[0,0,1]
	v_cvt_pk_fp8_f32 v3, v186, v187 op_sel:[0,0,1]
	v_cvt_pk_fp8_f32 v4, v182, v183 op_sel:[0,0,1]
	v_cvt_pk_fp8_f32 v5, v178, v179 op_sel:[0,0,1]
	v_lshl_add_u32 v8, s46, 8, v237
	v_lshlrev_b64 v[0:1], 11, v[6:7]
	v_ashrrev_i32_e32 v9, 31, v8
	v_lshl_add_u64 v[0:1], s[10:11], 0, v[0:1]
	v_lshl_add_u64 v[0:1], v[0:1], 0, v[8:9]
	global_store_dwordx4 v[0:1], v[2:5], off
	s_nop 1
	v_cvt_pk_fp8_f32 v2, v172, v173
	v_cvt_pk_fp8_f32 v3, v168, v169
	v_cvt_pk_fp8_f32 v4, v164, v165
	v_cvt_pk_fp8_f32 v5, v160, v161
	v_or_b32_e32 v10, 16, v6
	v_ashrrev_i32_e32 v11, 31, v10
	v_cvt_pk_fp8_f32 v2, v174, v175 op_sel:[0,0,1]
	v_cvt_pk_fp8_f32 v3, v170, v171 op_sel:[0,0,1]
	v_cvt_pk_fp8_f32 v4, v166, v167 op_sel:[0,0,1]
	v_cvt_pk_fp8_f32 v5, v162, v163 op_sel:[0,0,1]
	v_lshlrev_b64 v[10:11], 11, v[10:11]
	v_lshl_add_u64 v[10:11], s[10:11], 0, v[10:11]
	v_lshl_add_u64 v[10:11], v[10:11], 0, v[8:9]
	global_store_dwordx4 v[10:11], v[2:5], off
	s_nop 1
	v_cvt_pk_fp8_f32 v2, v156, v157
	v_cvt_pk_fp8_f32 v3, v152, v153
	v_cvt_pk_fp8_f32 v4, v148, v149
	v_cvt_pk_fp8_f32 v5, v144, v145
	v_or_b32_e32 v10, 32, v6
	v_ashrrev_i32_e32 v11, 31, v10
	v_cvt_pk_fp8_f32 v2, v158, v159 op_sel:[0,0,1]
	v_cvt_pk_fp8_f32 v3, v154, v155 op_sel:[0,0,1]
	v_cvt_pk_fp8_f32 v4, v150, v151 op_sel:[0,0,1]
	v_cvt_pk_fp8_f32 v5, v146, v147 op_sel:[0,0,1]
	v_lshlrev_b64 v[10:11], 11, v[10:11]
	v_lshl_add_u64 v[10:11], s[10:11], 0, v[10:11]
	v_lshl_add_u64 v[10:11], v[10:11], 0, v[8:9]
	global_store_dwordx4 v[10:11], v[2:5], off
	s_nop 1
	v_cvt_pk_fp8_f32 v2, v140, v141
	v_cvt_pk_fp8_f32 v3, v136, v137
	v_cvt_pk_fp8_f32 v4, v132, v133
	v_cvt_pk_fp8_f32 v5, v128, v129
	v_or_b32_e32 v6, 48, v6
	v_ashrrev_i32_e32 v7, 31, v6
	v_cvt_pk_fp8_f32 v2, v142, v143 op_sel:[0,0,1]
	v_cvt_pk_fp8_f32 v3, v138, v139 op_sel:[0,0,1]
	v_cvt_pk_fp8_f32 v4, v134, v135 op_sel:[0,0,1]
	v_cvt_pk_fp8_f32 v5, v130, v131 op_sel:[0,0,1]
	v_lshlrev_b64 v[6:7], 11, v[6:7]
	v_lshl_add_u64 v[6:7], s[10:11], 0, v[6:7]
	v_lshl_add_u64 v[6:7], v[6:7], 0, v[8:9]
	global_store_dwordx4 v[6:7], v[2:5], off
	s_nop 1
	v_cvt_pk_fp8_f32 v2, v124, v125
	v_cvt_pk_fp8_f32 v3, v120, v121
	v_cvt_pk_fp8_f32 v4, v116, v117
	v_cvt_pk_fp8_f32 v5, v112, v113
	v_cvt_pk_fp8_f32 v2, v126, v127 op_sel:[0,0,1]
	v_cvt_pk_fp8_f32 v3, v122, v123 op_sel:[0,0,1]
	v_cvt_pk_fp8_f32 v4, v118, v119 op_sel:[0,0,1]
	v_cvt_pk_fp8_f32 v5, v114, v115 op_sel:[0,0,1]
	v_add_co_u32_e32 v6, vcc, s23, v0
	s_nop 0
	v_addc_co_u32_e32 v7, vcc, 0, v1, vcc
	global_store_dwordx4 v[6:7], v[2:5], off
	s_nop 1
	v_cvt_pk_fp8_f32 v2, v108, v109
	v_cvt_pk_fp8_f32 v3, v104, v105
	v_cvt_pk_fp8_f32 v4, v100, v101
	v_cvt_pk_fp8_f32 v5, v96, v97
	v_cvt_pk_fp8_f32 v2, v110, v111 op_sel:[0,0,1]
	v_cvt_pk_fp8_f32 v3, v106, v107 op_sel:[0,0,1]
	v_cvt_pk_fp8_f32 v4, v102, v103 op_sel:[0,0,1]
	v_cvt_pk_fp8_f32 v5, v98, v99 op_sel:[0,0,1]
	v_add_co_u32_e32 v6, vcc, s28, v0
	s_nop 0
	v_addc_co_u32_e32 v7, vcc, 0, v1, vcc
	global_store_dwordx4 v[6:7], v[2:5], off
	s_nop 1
	v_cvt_pk_fp8_f32 v2, v92, v93
	v_cvt_pk_fp8_f32 v3, v88, v89
	v_cvt_pk_fp8_f32 v4, v84, v85
	v_cvt_pk_fp8_f32 v5, v80, v81
	v_cvt_pk_fp8_f32 v2, v94, v95 op_sel:[0,0,1]
	v_cvt_pk_fp8_f32 v3, v90, v91 op_sel:[0,0,1]
	v_cvt_pk_fp8_f32 v4, v86, v87 op_sel:[0,0,1]
	v_cvt_pk_fp8_f32 v5, v82, v83 op_sel:[0,0,1]
	v_add_co_u32_e32 v6, vcc, s3, v0
	s_nop 0
	v_addc_co_u32_e32 v7, vcc, 0, v1, vcc
	global_store_dwordx4 v[6:7], v[2:5], off
	s_nop 1
	v_cvt_pk_fp8_f32 v2, v76, v77
	v_cvt_pk_fp8_f32 v3, v72, v73
	v_cvt_pk_fp8_f32 v4, v68, v69
	v_cvt_pk_fp8_f32 v5, v64, v65
	v_cvt_pk_fp8_f32 v2, v78, v79 op_sel:[0,0,1]
	v_cvt_pk_fp8_f32 v3, v74, v75 op_sel:[0,0,1]
	v_cvt_pk_fp8_f32 v4, v70, v71 op_sel:[0,0,1]
	v_cvt_pk_fp8_f32 v5, v66, v67 op_sel:[0,0,1]
	v_add_co_u32_e32 v0, vcc, 0x58000, v0
	s_mov_b64 s[12:13], -1
	s_nop 0
	v_addc_co_u32_e32 v1, vcc, 0, v1, vcc
	s_andn2_b64 vcc, exec, s[42:43]
	global_store_dwordx4 v[0:1], v[2:5], off
	s_nop 1
	s_cbranch_vccnz .LBB0_1149
	s_andn2_b64 vcc, exec, s[8:9]
	s_cbranch_vccnz .LBB0_1148
	s_barrier
	s_branch .LBB0_1148
